# attention latent loop: threshold test against a scalar threshold copy set to -inf by the re-reference paths (replaces lane-mask AND)
# speedup vs baseline: 1.0214x; 1.0008x over previous
.LBB0_783:
	s_and_b64 vcc, exec, s[0:1]
	s_cbranch_vccz .LBB0_762
	s_ashr_i32 s0, s16, 7
	s_lshl_b32 s18, s0, 11
	s_and_b32 s1, s17, 0x780
	s_or_b32 s17, s18, s1
	s_lshl_b32 s1, s16, 3
	s_and_b32 s1, s1, 0x380
	v_mbcnt_lo_u32_b32 v171, -1, 0
	v_mbcnt_hi_u32_b32 v171, -1, v171
	s_lshl_b32 s96, s1, 1
	v_lshlrev_b32_e32 v20, 3, v171
	v_and_b32_e32 v0, 0x78, v20
	s_add_u32 s20, s6, s96
	v_lshlrev_b32_e32 v16, 1, v0
	s_addc_u32 s21, s7, 0
	v_mov_b32_e32 v17, v113
	v_add_u32_e32 v172, s4, v171
	v_lshl_add_u64 v[166:167], s[20:21], 0, v[16:17]
	s_add_u32 s20, s8, s96
	v_ashrrev_i32_e32 v181, 4, v172
	s_addc_u32 s21, s9, 0
	v_lshl_add_u64 v[168:169], s[20:21], 0, v[16:17]
	v_mad_u32_u24 v241, v181, s62, v16
	v_add_u32_e32 v34, s18, v181
	v_mad_i64_i32 v[0:1], s[20:21], v34, s62, v[168:169]
	v_add_co_u32_e32 v4, vcc, s74, v0
	v_mad_i64_i32 v[8:9], s[20:21], v34, s62, v[166:167]
	s_nop 0
	v_addc_co_u32_e32 v5, vcc, 0, v1, vcc
	v_add_co_u32_e32 v12, vcc, s74, v8
	global_load_dwordx4 v[0:3], v[0:1], off
	s_nop 0
	global_load_dwordx4 v[4:7], v[4:5], off
	v_addc_co_u32_e32 v13, vcc, 0, v9, vcc
	global_load_dwordx4 v[8:11], v[8:9], off
	s_nop 0
	global_load_dwordx4 v[12:15], v[12:13], off
	v_lshrrev_b32_e32 v17, 1, v172
	v_and_b32_e32 v173, 31, v171
	v_and_b32_e32 v176, 0x60, v17
	v_mov_b64_e32 v[18:19], s[50:51]
	v_ashrrev_i32_e32 v175, 8, v172
	v_or3_b32 v29, v173, s17, v176
	v_bfe_u32 v22, v20, 5, 2
	v_lshlrev_b32_e32 v20, 6, v175
	v_mad_i64_i32 v[18:19], s[20:21], v29, s62, v[18:19]
	v_bfe_u32 v174, v171, 5, 1
	v_ashrrev_i32_e32 v21, 31, v20
	v_lshl_add_u64 v[18:19], v[18:19], 0, s[96:97]
	v_lshlrev_b32_e32 v112, 4, v174
	v_lshl_add_u64 v[18:19], v[20:21], 1, v[18:19]
	v_lshl_add_u64 v[18:19], v[18:19], 0, v[112:113]
	global_load_dwordx4 v[122:125], v[18:19], off
	global_load_dwordx4 v[126:129], v[18:19], off offset:32
	global_load_dwordx4 v[118:121], v[18:19], off offset:64
	global_load_dwordx4 v[114:117], v[18:19], off offset:96
	v_and_b32_e32 v17, 0xfffff0, v181
	v_lshlrev_b32_e32 v24, 1, v181
	v_add_u32_e32 v27, 32, v181
	v_lshrrev_b32_e32 v25, 1, v181
	v_and_b32_e32 v26, 3, v181
	v_and_or_b32 v17, v181, 8, v17
	v_and_b32_e32 v20, 0xfffff0, v27
	v_lshlrev_b32_e32 v21, 1, v27
	v_and_b32_e32 v23, 0x70, v172
	v_lshlrev_b32_e32 v28, 8, v181
	v_and_or_b32 v24, v181, 4, v26
	v_lshlrev_b32_e32 v26, 8, v27
	v_lshrrev_b32_e32 v17, 1, v17
	v_and_or_b32 v20, v27, 8, v20
	v_and_b32_e32 v25, 48, v16
	v_bitop3_b32 v182, v16, v28, v23 bitop3:0xde
	v_bitop3_b32 v183, v26, v16, v23 bitop3:0xf6
	v_and_b32_e32 v243, 16, v181
	v_lshlrev_b32_e32 v243, 3, v243
	v_xor_b32_e32 v182, v243, v182
	v_xor_b32_e32 v183, v243, v183
	v_or_b32_e32 v16, v17, v22
	v_lshrrev_b32_e32 v17, 1, v20
	v_lshlrev_b32_e32 v24, 6, v24
	v_lshlrev_b32_e32 v16, 9, v16
	v_or_b32_e32 v17, v17, v22
	v_or3_b32 v184, v16, v24, v25
	v_lshlrev_b32_e32 v16, 9, v17
	v_or3_b32 v185, v16, v24, v25
	v_add_u32_e32 v32, 0, v184
	v_add_u32_e32 v21, 0, v182
	v_add_u32_e32 v20, 0, v183
	v_add_u32_e32 v33, 0, v185
	s_waitcnt vmcnt(0)
	v_lshlrev_b32_e32 v38, 7, v175
	v_lshlrev_b32_e32 v189, 8, v173
	v_add_u32_e32 v191, 0, v189
	s_movk_i32 s1, 0x60
	s_waitcnt vmcnt(7)
	ds_write_b128 v32, v[0:3] offset:1024
	s_waitcnt vmcnt(6)
	ds_write_b128 v33, v[4:7] offset:1024
	s_waitcnt vmcnt(5)
	ds_write_b128 v21, v[8:11] offset:50176
	s_waitcnt vmcnt(4)
	ds_write_b128 v20, v[12:15] offset:50176
	v_add_u32_e32 v4, 64, v34
	v_mad_i64_i32 v[0:1], s[20:21], v4, s62, v[168:169]
	v_add_co_u32_e32 v2, vcc, s74, v0
	s_nop 1
	v_addc_co_u32_e32 v3, vcc, 0, v1, vcc
	global_load_dwordx4 v[16:19], v[0:1], off
	global_load_dwordx4 v[20:23], v[2:3], off
	v_mad_i64_i32 v[0:1], s[20:21], v4, s62, v[166:167]
	v_add_co_u32_e32 v2, vcc, s74, v0
	v_add_u32_e32 v4, 0x80, v34
	s_nop 0
	v_addc_co_u32_e32 v3, vcc, 0, v1, vcc
	global_load_dwordx4 v[24:27], v[0:1], off
	global_load_dwordx4 v[28:31], v[2:3], off
	v_mad_i64_i32 v[0:1], s[20:21], v4, s62, v[166:167]
	v_add_co_u32_e32 v2, vcc, s74, v0
	s_nop 1
	v_addc_co_u32_e32 v3, vcc, 0, v1, vcc
	global_load_dwordx4 v[142:145], v[2:3], off
	global_load_dwordx4 v[138:141], v[0:1], off
	v_mad_i64_i32 v[0:1], s[20:21], v4, s62, v[168:169]
	v_add_co_u32_e32 v2, vcc, s74, v0
	s_nop 1
	v_addc_co_u32_e32 v3, vcc, 0, v1, vcc
	global_load_dwordx4 v[134:137], v[2:3], off
	global_load_dwordx4 v[130:133], v[0:1], off
	v_lshlrev_b32_e32 v0, 4, v171
	v_and_b32_e32 v39, 0x70, v0
	v_bitop3_b32 v190, v38, v39, v112 bitop3:0x36
	v_and_b32_e32 v244, 16, v171
	v_lshlrev_b32_e32 v244, 3, v244
	v_xor_b32_e32 v190, v244, v190
	v_add_u32_e32 v34, v191, v190
	s_waitcnt lgkmcnt(0)
	s_barrier
	ds_read_b128 v[0:3], v34 offset:50176
	ds_read_b128 v[34:37], v34 offset:58368
	v_or_b32_e32 v38, v38, v112
	v_bitop3_b32 v188, v38, v39, 32 bitop3:0x36
	v_xor_b32_e32 v188, v244, v188
	v_add_u32_e32 v40, v191, v188
	s_waitcnt vmcnt(11) lgkmcnt(0)
	v_mfma_f32_32x32x16_bf16 v[64:79], v[34:37], v[122:125], 0
	ds_read_b128 v[34:37], v40 offset:50176
	v_bitop3_b32 v187, v38, v39, 64 bitop3:0x36
	v_bitop3_b32 v186, v38, v39, s1 bitop3:0x36
	v_xor_b32_e32 v187, v244, v187
	v_xor_b32_e32 v186, v244, v186
	v_add_u32_e32 v38, v191, v186
	v_mfma_f32_32x32x16_bf16 v[0:15], v[0:3], v[122:125], 0
	s_waitcnt vmcnt(10) lgkmcnt(0)
	v_mfma_f32_32x32x16_bf16 v[0:15], v[34:37], v[126:129], v[0:15]
	ds_read_b128 v[34:37], v40 offset:58368
	v_add_u32_e32 v40, v191, v187
	s_waitcnt lgkmcnt(0)
	v_mfma_f32_32x32x16_bf16 v[64:79], v[34:37], v[126:129], v[64:79]
	ds_read_b128 v[34:37], v40 offset:50176
	s_waitcnt vmcnt(9) lgkmcnt(0)
	v_mfma_f32_32x32x16_bf16 v[0:15], v[34:37], v[118:121], v[0:15]
	ds_read_b128 v[34:37], v40 offset:58368
	s_waitcnt lgkmcnt(0)
	v_mfma_f32_32x32x16_bf16 v[64:79], v[34:37], v[118:121], v[64:79]
	ds_read_b128 v[34:37], v38 offset:50176
	s_waitcnt vmcnt(8) lgkmcnt(0)
	v_mfma_f32_32x32x16_bf16 v[0:15], v[34:37], v[114:117], v[0:15]
	ds_read_b128 v[34:37], v38 offset:58368
	s_waitcnt lgkmcnt(0)
	v_mfma_f32_32x32x16_bf16 v[64:79], v[34:37], v[114:117], v[64:79]
	s_nop 8
	v_max_f32_e32 v34, v1, v1
	v_max_f32_e32 v35, v0, v0
	v_max_f32_e32 v34, v35, v34
	v_max3_f32 v34, v34, v2, v3
	v_max3_f32 v34, v34, v4, v5
	v_max3_f32 v34, v34, v6, v7
	v_max3_f32 v34, v34, v8, v9
	v_max3_f32 v34, v34, v10, v11
	v_max3_f32 v34, v34, v12, v13
	v_max3_f32 v34, v34, v14, v15
	v_max3_f32 v34, v34, v64, v65
	v_max3_f32 v34, v34, v66, v67
	v_max3_f32 v34, v34, v68, v69
	v_max3_f32 v34, v34, v70, v71
	v_max3_f32 v34, v34, v72, v73
	v_max3_f32 v34, v34, v74, v75
	v_max3_f32 v34, v34, v76, v77
	v_max3_f32 v34, v34, v78, v79
	v_mov_b32_e32 v35, v34
	s_nop 1
	v_permlane32_swap_b32_e32 v34, v35
	v_max_f32_e32 v35, v35, v35
	v_max_f32_e32 v34, v34, v34
	v_max_f32_e32 v34, v34, v35
	v_cmp_ge_f32_e32 vcc, s75, v34
	s_cmp_eq_u64 vcc, exec
	s_cbranch_scc0 .LBB0_814
	v_mov_b32_e32 v193, 1.0
	v_mov_b32_e32 v164, 0
	s_mov_b32 s56, s75

.LBB0_787:
	v_add_u32_e32 v180, s21, v191
	v_add_u32_e32 v84, v180, v190
	ds_read_b128 v[80:83], v84 offset:50176
	ds_read_b128 v[84:87], v84 offset:58368
	v_add_u32_e32 v195, v180, v188
	ds_read_b128 v[196:199], v195 offset:50176
	ds_read_b128 v[200:203], v195 offset:58368
	v_add_u32_e32 v195, v180, v187
	s_waitcnt lgkmcnt(2)
	v_mfma_f32_32x32x16_bf16 v[96:111], v[80:83], v[122:125], 0
	v_add_u32_e32 v180, v180, v186
	v_exp_f32_e32 v204, v72
	v_exp_f32_e32 v205, v73
	v_exp_f32_e32 v206, v74
	v_exp_f32_e32 v207, v75
	v_exp_f32_e32 v208, v76
	v_exp_f32_e32 v209, v77
	v_mfma_f32_32x32x16_bf16 v[80:95], v[84:87], v[122:125], 0
	v_exp_f32_e32 v210, v78
	v_exp_f32_e32 v79, v79
	s_waitcnt lgkmcnt(0)
	v_mfma_f32_32x32x16_bf16 v[96:111], v[196:199], v[126:129], v[96:111]
	v_mfma_f32_32x32x16_bf16 v[80:95], v[200:203], v[126:129], v[80:95]
	ds_read_b128 v[196:199], v195 offset:50176
	ds_read_b128 v[200:203], v195 offset:58368
	s_waitcnt lgkmcnt(0)
	v_mfma_f32_32x32x16_bf16 v[96:111], v[196:199], v[118:121], v[96:111]
	v_mfma_f32_32x32x16_bf16 v[80:95], v[200:203], v[118:121], v[80:95]
	ds_read_b128 v[196:199], v180 offset:50176
	ds_read_b128 v[200:203], v180 offset:58368
	v_exp_f32_e32 v180, v64
	v_add_f32_e32 v64, v161, v159
	v_add_f32_e32 v195, v157, v160
	v_add_f32_e32 v64, v155, v64
	v_add_f32_e32 v195, v158, v195
	v_add_f32_e32 v64, v154, v64
	v_add_f32_e32 v195, v156, v195
	v_add_f32_e32 v64, v151, v64
	v_add_f32_e32 v195, v153, v195
	v_add_f32_e32 v64, v149, v64
	v_add_f32_e32 v195, v152, v195
	v_add_f32_e32 v64, v147, v64
	s_waitcnt lgkmcnt(0)
	v_mfma_f32_32x32x16_bf16 v[96:111], v[196:199], v[114:117], v[96:111]
	v_exp_f32_e32 v197, v65
	v_add_f32_e32 v195, v150, v195
	v_exp_f32_e32 v198, v66
	v_add_f32_e32 v64, v146, v64
	v_exp_f32_e32 v199, v67
	v_add_f32_e32 v195, v148, v195
	v_add_f32_e32 v64, v180, v64
	v_mfma_f32_32x32x16_bf16 v[80:95], v[200:203], v[114:117], v[80:95]
	v_exp_f32_e32 v200, v68
	v_exp_f32_e32 v201, v69
	v_add_f32_e32 v195, v197, v195
	v_exp_f32_e32 v202, v70
	v_add_f32_e32 v64, v198, v64
	v_exp_f32_e32 v203, v71
	v_add_f32_e32 v195, v199, v195
	v_add_f32_e32 v64, v200, v64
	v_add_f32_e32 v195, v201, v195
	v_add_f32_e32 v64, v202, v64
	v_add_f32_e32 v195, v203, v195
	v_add_f32_e32 v64, v204, v64
	v_add_f32_e32 v195, v205, v195
	v_add_f32_e32 v64, v206, v64
	v_add_f32_e32 v195, v207, v195
	v_add_f32_e32 v64, v208, v64
	v_add_f32_e32 v195, v209, v195
	v_add_f32_e32 v64, v210, v64
	v_add_f32_e32 v195, v79, v195
	v_add_f32_e32 v195, v195, v64
	v_cvt_pk_bf16_f32 v64, v159, v161
	v_cvt_pk_bf16_f32 v65, v157, v160
	v_cvt_pk_bf16_f32 v66, v155, v158
	v_cvt_pk_bf16_f32 v67, v154, v156
	v_cvt_pk_bf16_f32 v68, v151, v153
	v_cvt_pk_bf16_f32 v69, v149, v152
	v_cvt_pk_bf16_f32 v70, v147, v150
	v_cvt_pk_bf16_f32 v71, v146, v148
	v_cvt_pk_bf16_f32 v72, v180, v197
	v_cvt_pk_bf16_f32 v73, v198, v199
	v_cvt_pk_bf16_f32 v74, v200, v201
	v_cvt_pk_bf16_f32 v75, v202, v203
	v_cvt_pk_bf16_f32 v76, v204, v205
	v_cvt_pk_bf16_f32 v77, v206, v207
	v_cvt_pk_bf16_f32 v78, v208, v209
	v_cvt_pk_bf16_f32 v79, v210, v79
	s_add_u32 s66, s78, s65
	s_addc_u32 s67, s79, 0
	s_add_i32 s85, s22, s84
	s_add_i32 m0, s85, 0x400
	s_add_i32 s86, s20, s84
	global_load_lds_dwordx4 v185, s[66:67]
	s_add_i32 m0, s85, 0x2400
	s_add_i32 s64, s65, 0x60000
	global_load_lds_dwordx4 v184, s[66:67]
	s_add_i32 m0, s86, 0xc400
	s_add_u32 s70, s80, s64
	s_addc_u32 s71, s81, 0
	global_load_lds_dwordx4 v183, s[70:71]
	s_add_i32 m0, s86, 0xe400
	s_mov_b32 s65, s64
	global_load_lds_dwordx4 v182, s[70:71]
	v_add_u32_e32 v180, s20, v194
	ds_read_b64_tr_b16 v[198:199], v180 offset:0
	ds_read_b64_tr_b16 v[200:201], v180 offset:0x800
	ds_read_b64_tr_b16 v[202:203], v180 offset:0x1000
	ds_read_b64_tr_b16 v[204:205], v180 offset:0x1800
	ds_read_b64_tr_b16 v[206:207], v180 offset:0x2000
	ds_read_b64_tr_b16 v[208:209], v180 offset:0x2800
	ds_read_b64_tr_b16 v[222:223], v180 offset:0x3000
	ds_read_b64_tr_b16 v[224:225], v180 offset:0x3800
	s_waitcnt lgkmcnt(0)
	v_mfma_f32_32x32x16_bf16 v[0:15], v[64:67], v[198:201], v[0:15]
	ds_read_b64_tr_b16 v[198:199], v180 offset:0x200
	ds_read_b64_tr_b16 v[200:201], v180 offset:0xa00
	v_mfma_f32_32x32x16_bf16 v[0:15], v[68:71], v[202:205], v[0:15]
	ds_read_b64_tr_b16 v[202:203], v180 offset:0x1200
	ds_read_b64_tr_b16 v[204:205], v180 offset:0x1a00
	v_mfma_f32_32x32x16_bf16 v[0:15], v[72:75], v[206:209], v[0:15]
	ds_read_b64_tr_b16 v[206:207], v180 offset:0x2200
	ds_read_b64_tr_b16 v[208:209], v180 offset:0x2a00
	v_mfma_f32_32x32x16_bf16 v[0:15], v[76:79], v[222:225], v[0:15]
	ds_read_b64_tr_b16 v[222:223], v180 offset:0x3200
	ds_read_b64_tr_b16 v[224:225], v180 offset:0x3a00
	s_waitcnt lgkmcnt(0)
	v_mfma_f32_32x32x16_bf16 v[48:63], v[64:67], v[198:201], v[48:63]
	ds_read_b64_tr_b16 v[198:199], v180 offset:0x400
	ds_read_b64_tr_b16 v[200:201], v180 offset:0xc00
	v_mfma_f32_32x32x16_bf16 v[48:63], v[68:71], v[202:205], v[48:63]
	ds_read_b64_tr_b16 v[202:203], v180 offset:0x1400
	ds_read_b64_tr_b16 v[204:205], v180 offset:0x1c00
	v_mfma_f32_32x32x16_bf16 v[48:63], v[72:75], v[206:209], v[48:63]
	ds_read_b64_tr_b16 v[206:207], v180 offset:0x2400
	ds_read_b64_tr_b16 v[208:209], v180 offset:0x2c00
	v_mfma_f32_32x32x16_bf16 v[48:63], v[76:79], v[222:225], v[48:63]
	ds_read_b64_tr_b16 v[222:223], v180 offset:0x3400
	ds_read_b64_tr_b16 v[224:225], v180 offset:0x3c00
	s_waitcnt lgkmcnt(0)
	v_mfma_f32_32x32x16_bf16 v[32:47], v[64:67], v[198:201], v[32:47]
	ds_read_b64_tr_b16 v[198:199], v180 offset:0x600
	ds_read_b64_tr_b16 v[200:201], v180 offset:0xe00
	v_mfma_f32_32x32x16_bf16 v[32:47], v[68:71], v[202:205], v[32:47]
	ds_read_b64_tr_b16 v[202:203], v180 offset:0x1600
	ds_read_b64_tr_b16 v[204:205], v180 offset:0x1e00
	v_mfma_f32_32x32x16_bf16 v[32:47], v[72:75], v[206:209], v[32:47]
	ds_read_b64_tr_b16 v[206:207], v180 offset:0x2600
	ds_read_b64_tr_b16 v[208:209], v180 offset:0x2e00
	v_mfma_f32_32x32x16_bf16 v[32:47], v[76:79], v[222:225], v[32:47]
	ds_read_b64_tr_b16 v[222:223], v180 offset:0x3600
	ds_read_b64_tr_b16 v[224:225], v180 offset:0x3e00
	s_waitcnt lgkmcnt(0)
	v_mfma_f32_32x32x16_bf16 v[16:31], v[64:67], v[198:201], v[16:31]
	v_max_f32_e32 v64, v96, v97
	v_max3_f32 v65, v80, v81, v82
	v_max3_f32 v64, v64, v98, v99
	v_max3_f32 v65, v65, v83, v84
	v_max3_f32 v64, v64, v100, v101
	v_mfma_f32_32x32x16_bf16 v[16:31], v[68:71], v[202:205], v[16:31]
	v_max3_f32 v65, v65, v85, v86
	v_max3_f32 v64, v64, v102, v103
	v_max3_f32 v65, v65, v87, v88
	v_max3_f32 v64, v64, v104, v105
	v_max3_f32 v65, v65, v89, v90
	v_max3_f32 v64, v64, v106, v107
	v_max3_f32 v65, v65, v91, v92
	v_mfma_f32_32x32x16_bf16 v[16:31], v[72:75], v[206:209], v[16:31]
	v_max3_f32 v64, v64, v108, v109
	v_max3_f32 v65, v65, v93, v94
	v_max3_f32 v64, v64, v110, v111
	v_max3_f32 v64, v64, v65, v95
	v_mov_b32_e32 v198, 1.0
	v_mfma_f32_32x32x16_bf16 v[16:31], v[76:79], v[222:225], v[16:31]
	v_cmp_ge_f32_e64 s[0:1], s56, v64
	s_cmp_eq_u64 s[0:1], exec
	s_cbranch_scc1 .LBB0_792
	s_branch .LBB0_801

.LBB0_794:
	v_add_u32_e32 v197, s21, v194
	ds_read_b64_tr_b16 v[202:203], v197 offset:0
	ds_read_b64_tr_b16 v[204:205], v197 offset:0x800
	ds_read_b64_tr_b16 v[206:207], v197 offset:0x1000
	ds_read_b64_tr_b16 v[208:209], v197 offset:0x1800
	ds_read_b64_tr_b16 v[222:223], v197 offset:0x2000
	ds_read_b64_tr_b16 v[224:225], v197 offset:0x2800
	ds_read_b64_tr_b16 v[226:227], v197 offset:0x3000
	ds_read_b64_tr_b16 v[228:229], v197 offset:0x3800
	s_waitcnt lgkmcnt(0)
	v_mfma_f32_32x32x16_bf16 v[0:15], v[80:83], v[202:205], v[0:15]
	ds_read_b64_tr_b16 v[202:203], v197 offset:0x200
	ds_read_b64_tr_b16 v[204:205], v197 offset:0xa00
	v_mfma_f32_32x32x16_bf16 v[0:15], v[84:87], v[206:209], v[0:15]
	ds_read_b64_tr_b16 v[206:207], v197 offset:0x1200
	ds_read_b64_tr_b16 v[208:209], v197 offset:0x1a00
	v_mfma_f32_32x32x16_bf16 v[0:15], v[88:91], v[222:225], v[0:15]
	ds_read_b64_tr_b16 v[222:223], v197 offset:0x2200
	ds_read_b64_tr_b16 v[224:225], v197 offset:0x2a00
	v_mfma_f32_32x32x16_bf16 v[0:15], v[92:95], v[226:229], v[0:15]
	ds_read_b64_tr_b16 v[226:227], v197 offset:0x3200
	ds_read_b64_tr_b16 v[228:229], v197 offset:0x3a00
	s_waitcnt lgkmcnt(0)
	v_mfma_f32_32x32x16_bf16 v[48:63], v[80:83], v[202:205], v[48:63]
	ds_read_b64_tr_b16 v[202:203], v197 offset:0x400
	ds_read_b64_tr_b16 v[204:205], v197 offset:0xc00
	v_mfma_f32_32x32x16_bf16 v[48:63], v[84:87], v[206:209], v[48:63]
	ds_read_b64_tr_b16 v[206:207], v197 offset:0x1400
	ds_read_b64_tr_b16 v[208:209], v197 offset:0x1c00
	v_mfma_f32_32x32x16_bf16 v[48:63], v[88:91], v[222:225], v[48:63]
	ds_read_b64_tr_b16 v[222:223], v197 offset:0x2400
	ds_read_b64_tr_b16 v[224:225], v197 offset:0x2c00
	v_mfma_f32_32x32x16_bf16 v[48:63], v[92:95], v[226:229], v[48:63]
	ds_read_b64_tr_b16 v[226:227], v197 offset:0x3400
	ds_read_b64_tr_b16 v[228:229], v197 offset:0x3c00
	s_waitcnt lgkmcnt(0)
	v_mfma_f32_32x32x16_bf16 v[32:47], v[80:83], v[202:205], v[32:47]
	ds_read_b64_tr_b16 v[202:203], v197 offset:0x600
	ds_read_b64_tr_b16 v[204:205], v197 offset:0xe00
	v_mfma_f32_32x32x16_bf16 v[32:47], v[84:87], v[206:209], v[32:47]
	ds_read_b64_tr_b16 v[206:207], v197 offset:0x1600
	ds_read_b64_tr_b16 v[208:209], v197 offset:0x1e00
	v_mfma_f32_32x32x16_bf16 v[32:47], v[88:91], v[222:225], v[32:47]
	ds_read_b64_tr_b16 v[222:223], v197 offset:0x2600
	ds_read_b64_tr_b16 v[224:225], v197 offset:0x2e00
	v_mfma_f32_32x32x16_bf16 v[32:47], v[92:95], v[226:229], v[32:47]
	ds_read_b64_tr_b16 v[226:227], v197 offset:0x3600
	ds_read_b64_tr_b16 v[228:229], v197 offset:0x3e00
	s_waitcnt lgkmcnt(0)
	v_mfma_f32_32x32x16_bf16 v[16:31], v[80:83], v[202:205], v[16:31]
	v_max_f32_e32 v80, v96, v97
	v_max3_f32 v81, v64, v65, v66
	v_max3_f32 v80, v80, v98, v99
	v_max3_f32 v81, v81, v67, v68
	v_max3_f32 v80, v80, v100, v101
	v_mfma_f32_32x32x16_bf16 v[16:31], v[84:87], v[206:209], v[16:31]
	v_max3_f32 v81, v81, v69, v70
	v_max3_f32 v80, v80, v102, v103
	v_max3_f32 v81, v81, v71, v72
	v_max3_f32 v80, v80, v104, v105
	v_max3_f32 v81, v81, v73, v74
	v_max3_f32 v80, v80, v106, v107
	v_max3_f32 v81, v81, v75, v76
	v_mfma_f32_32x32x16_bf16 v[16:31], v[88:91], v[222:225], v[16:31]
	v_max3_f32 v80, v80, v108, v109
	v_max3_f32 v81, v81, v77, v78
	v_max3_f32 v80, v80, v110, v111
	v_max3_f32 v80, v80, v81, v79
	v_mov_b32_e32 v197, 1.0
	v_mfma_f32_32x32x16_bf16 v[16:31], v[92:95], v[226:229], v[16:31]
	v_cmp_ge_f32_e64 s[0:1], s56, v80
	s_cmp_eq_u64 s[0:1], exec
	s_cbranch_scc1 .LBB0_799
	s_branch .LBB0_802

.LBB0_801:
	v_mov_b32_e32 v65, v64
	s_nop 1
	v_permlane32_swap_b32_e32 v64, v65
	v_max_f32_e32 v64, v64, v65
	v_sub_f32_e32 v65, v64, v164
	v_cmp_lt_f32_e32 vcc, s75, v65
	v_max_f32_e32 v64, v64, v64
	v_max_f32_e32 v65, v164, v164
	v_max_f32_e32 v64, v65, v64
	v_cndmask_b32_e32 v64, v164, v64, vcc
	v_sub_f32_e32 v65, v164, v64
	v_exp_f32_e32 v198, v65
	v_pk_add_f32 v[96:97], v[96:97], v[64:65] op_sel_hi:[1,0] neg_lo:[0,1] neg_hi:[0,1]
	v_pk_add_f32 v[98:99], v[98:99], v[64:65] op_sel_hi:[1,0] neg_lo:[0,1] neg_hi:[0,1]
	v_pk_add_f32 v[100:101], v[100:101], v[64:65] op_sel_hi:[1,0] neg_lo:[0,1] neg_hi:[0,1]
	v_pk_add_f32 v[102:103], v[102:103], v[64:65] op_sel_hi:[1,0] neg_lo:[0,1] neg_hi:[0,1]
	v_pk_add_f32 v[104:105], v[104:105], v[64:65] op_sel_hi:[1,0] neg_lo:[0,1] neg_hi:[0,1]
	v_pk_add_f32 v[106:107], v[106:107], v[64:65] op_sel_hi:[1,0] neg_lo:[0,1] neg_hi:[0,1]
	v_pk_add_f32 v[108:109], v[108:109], v[64:65] op_sel_hi:[1,0] neg_lo:[0,1] neg_hi:[0,1]
	v_pk_add_f32 v[110:111], v[110:111], v[64:65] op_sel_hi:[1,0] neg_lo:[0,1] neg_hi:[0,1]
	v_sub_f32_e32 v95, v95, v64
	v_sub_f32_e32 v94, v94, v64
	v_sub_f32_e32 v93, v93, v64
	v_sub_f32_e32 v92, v92, v64
	v_sub_f32_e32 v91, v91, v64
	v_sub_f32_e32 v90, v90, v64
	v_sub_f32_e32 v89, v89, v64
	v_sub_f32_e32 v88, v88, v64
	v_sub_f32_e32 v87, v87, v64
	v_sub_f32_e32 v86, v86, v64
	v_sub_f32_e32 v85, v85, v64
	v_sub_f32_e32 v84, v84, v64
	v_sub_f32_e32 v83, v83, v64
	v_sub_f32_e32 v82, v82, v64
	v_sub_f32_e32 v81, v81, v64
	v_sub_f32_e32 v80, v80, v64
	v_mov_b32_e32 v164, v64
	s_mov_b32 s56, 0xff800000
	s_branch .LBB0_788
.LBB0_802:
	v_mov_b32_e32 v81, v80
	s_nop 1
	v_permlane32_swap_b32_e32 v80, v81
	v_max_f32_e32 v80, v80, v81
	v_sub_f32_e32 v81, v80, v164
	v_cmp_lt_f32_e32 vcc, s75, v81
	v_max_f32_e32 v80, v80, v80
	v_max_f32_e32 v81, v164, v164
	v_max_f32_e32 v80, v81, v80
	v_cndmask_b32_e32 v80, v164, v80, vcc
	v_sub_f32_e32 v81, v164, v80
	v_exp_f32_e32 v197, v81
	v_pk_add_f32 v[96:97], v[96:97], v[80:81] op_sel_hi:[1,0] neg_lo:[0,1] neg_hi:[0,1]
	v_pk_add_f32 v[98:99], v[98:99], v[80:81] op_sel_hi:[1,0] neg_lo:[0,1] neg_hi:[0,1]
	v_pk_add_f32 v[100:101], v[100:101], v[80:81] op_sel_hi:[1,0] neg_lo:[0,1] neg_hi:[0,1]
	v_pk_add_f32 v[102:103], v[102:103], v[80:81] op_sel_hi:[1,0] neg_lo:[0,1] neg_hi:[0,1]
	v_pk_add_f32 v[104:105], v[104:105], v[80:81] op_sel_hi:[1,0] neg_lo:[0,1] neg_hi:[0,1]
	v_pk_add_f32 v[106:107], v[106:107], v[80:81] op_sel_hi:[1,0] neg_lo:[0,1] neg_hi:[0,1]
	v_pk_add_f32 v[108:109], v[108:109], v[80:81] op_sel_hi:[1,0] neg_lo:[0,1] neg_hi:[0,1]
	v_pk_add_f32 v[110:111], v[110:111], v[80:81] op_sel_hi:[1,0] neg_lo:[0,1] neg_hi:[0,1]
	v_sub_f32_e32 v79, v79, v80
	v_sub_f32_e32 v78, v78, v80
	v_sub_f32_e32 v77, v77, v80
	v_sub_f32_e32 v76, v76, v80
	v_sub_f32_e32 v75, v75, v80
	v_sub_f32_e32 v74, v74, v80
	v_sub_f32_e32 v73, v73, v80
	v_sub_f32_e32 v72, v72, v80
	v_sub_f32_e32 v71, v71, v80
	v_sub_f32_e32 v70, v70, v80
	v_sub_f32_e32 v69, v69, v80
	v_sub_f32_e32 v68, v68, v80
	v_sub_f32_e32 v67, v67, v80
	v_sub_f32_e32 v66, v66, v80
	v_sub_f32_e32 v65, v65, v80
	v_sub_f32_e32 v64, v64, v80
	v_mov_b32_e32 v164, v80
	s_mov_b32 s56, 0xff800000
	s_branch .LBB0_795

.LBB0_814:
	v_cmp_lt_f32_e32 vcc, s75, v34
	v_max_f32_e32 v34, v34, v34
	v_max_f32_e32 v34, 0, v34
	v_cndmask_b32_e32 v164, 0, v34, vcc
	s_mov_b32 s56, 0xff800000
	v_exp_f32_e64 v193, -v164
	v_pk_add_f32 v[0:1], v[0:1], v[164:165] op_sel_hi:[1,0] neg_lo:[0,1] neg_hi:[0,1]
	v_pk_add_f32 v[2:3], v[2:3], v[164:165] op_sel_hi:[1,0] neg_lo:[0,1] neg_hi:[0,1]
	v_pk_add_f32 v[4:5], v[4:5], v[164:165] op_sel_hi:[1,0] neg_lo:[0,1] neg_hi:[0,1]
	v_pk_add_f32 v[6:7], v[6:7], v[164:165] op_sel_hi:[1,0] neg_lo:[0,1] neg_hi:[0,1]
	v_pk_add_f32 v[8:9], v[8:9], v[164:165] op_sel_hi:[1,0] neg_lo:[0,1] neg_hi:[0,1]
	v_pk_add_f32 v[10:11], v[10:11], v[164:165] op_sel_hi:[1,0] neg_lo:[0,1] neg_hi:[0,1]
	v_pk_add_f32 v[12:13], v[12:13], v[164:165] op_sel_hi:[1,0] neg_lo:[0,1] neg_hi:[0,1]
	v_pk_add_f32 v[14:15], v[14:15], v[164:165] op_sel_hi:[1,0] neg_lo:[0,1] neg_hi:[0,1]
	v_sub_f32_e32 v79, v79, v164
	v_sub_f32_e32 v78, v78, v164
	v_sub_f32_e32 v77, v77, v164
	v_sub_f32_e32 v76, v76, v164
	v_sub_f32_e32 v75, v75, v164
	v_sub_f32_e32 v74, v74, v164
	v_sub_f32_e32 v73, v73, v164
	v_sub_f32_e32 v72, v72, v164
	v_sub_f32_e32 v71, v71, v164
	v_sub_f32_e32 v70, v70, v164
	v_sub_f32_e32 v69, v69, v164
	v_sub_f32_e32 v68, v68, v164
	v_sub_f32_e32 v67, v67, v164
	v_sub_f32_e32 v66, v66, v164
	v_sub_f32_e32 v65, v65, v164
	v_sub_f32_e32 v64, v64, v164
	s_branch .LBB0_786
